# baseline (speedup 1.0000x reference)
_Z12final_kernelPKfPKiPK15HIP_vector_typeIiLj4EES2_S2_S0_S0_S0_S0_Pf:
	s_load_dwordx2 s[4:5], s[0:1], 0x10
	s_ashr_i32 s3, s2, 31
	s_lshl_b64 s[6:7], s[2:3], 4
	s_waitcnt lgkmcnt(0)
	s_add_u32 s4, s4, s6
	s_addc_u32 s5, s5, s7
	s_load_dwordx4 s[4:7], s[4:5], 0x0
	s_waitcnt lgkmcnt(0)
	s_cmp_eq_u32 s6, 0
	s_cbranch_scc1 .LBB4_17
	s_load_dwordx2 s[12:13], s[0:1], 0x8
	s_load_dwordx2 s[18:19], s[0:1], 0x0
	s_load_dwordx4 s[8:11], s[0:1], 0x20
	s_load_dwordx2 s[16:17], s[0:1], 0x30
	s_load_dwordx4 s[36:39], s[0:1], 0x38
	s_load_dwordx2 s[40:41], s[0:1], 0x48
	s_movk_i32 s20, 0x51f
	s_add_i32 s21, s6, -1
	s_movk_i32 s34, 0x5556
	s_movk_i32 s35, 0x64
	v_add_u32_e32 v1, 0x100, v0
	v_add_u32_e32 v2, 0x200, v0
	v_add_u32_e32 v3, 0x300, v0
	v_min_u32_e32 v3, 0x31f, v3
	v_mul_u32_u24_e32 v4, s20, v0
	v_mul_u32_u24_e32 v5, s20, v1
	v_mul_u32_u24_e32 v6, s20, v2
	v_mul_u32_u24_e32 v7, s20, v3
	v_lshrrev_b32_e32 v4, 15, v4
	v_lshrrev_b32_e32 v5, 15, v5
	v_lshrrev_b32_e32 v6, 15, v6
	v_lshrrev_b32_e32 v7, 15, v7
	v_mul_u32_u24_e32 v8, 25, v4
	v_mul_u32_u24_e32 v9, 25, v5
	v_mul_u32_u24_e32 v10, 25, v6
	v_mul_u32_u24_e32 v11, 25, v7
	v_sub_u32_e32 v8, v0, v8
	v_sub_u32_e32 v9, v1, v9
	v_sub_u32_e32 v10, v2, v10
	v_sub_u32_e32 v11, v3, v11
	v_min_u32_e32 v12, s21, v4
	v_min_u32_e32 v13, s21, v5
	v_min_u32_e32 v14, s21, v6
	v_min_u32_e32 v15, s21, v7
	v_add_lshl_u32 v12, v12, s5, 2
	v_add_lshl_u32 v13, v13, s5, 2
	v_add_lshl_u32 v14, v14, s5, 2
	v_add_lshl_u32 v15, v15, s5, 2
	v_mul_u32_u24_e32 v130, s34, v0
	v_lshrrev_b32_e32 v130, 16, v130
	v_mul_u32_u24_e32 v131, 3, v130
	v_sub_u32_e32 v131, v0, v131
	v_min_u32_e32 v132, s21, v130
	v_add_lshl_u32 v132, v132, s5, 2
	v_lshlrev_b32_e32 v133, 2, v131
	v_min_u32_e32 v134, 0x4a, v0
	v_lshlrev_b32_e32 v134, 4, v134
	s_waitcnt lgkmcnt(0)
	s_mul_i32 s22, s4, 0x4b0
	s_add_u32 s36, s36, s22
	s_addc_u32 s37, s37, 0
	s_mul_i32 s22, s4, 12
	s_add_u32 s38, s38, s22
	s_addc_u32 s39, s39, 0
	global_load_dwordx4 v[124:127], v134, s[36:37]
	global_load_dword v128, v133, s[38:39]
	global_load_dword v129, v132, s[12:13]
	global_load_dword v12, v12, s[12:13]
	global_load_dword v13, v13, s[12:13]
	global_load_dword v14, v14, s[12:13]
	global_load_dword v15, v15, s[12:13]
	s_mul_i32 s22, s2, 0xc800
	s_add_u32 s24, s18, s22
	s_addc_u32 s25, s19, 0
	s_add_u32 s26, s24, 0x3200
	s_addc_u32 s27, s25, 0
	s_add_u32 s28, s24, 0x6400
	s_addc_u32 s29, s25, 0
	s_add_u32 s30, s24, 0x9600
	s_addc_u32 s31, s25, 0
	s_mul_i32 s22, s4, 0x190
	s_add_u32 s16, s16, s22
	s_addc_u32 s17, s17, 0
	s_mul_i32 s32, s4, 0x864
	s_addk_i32 s32, 0x800
	s_movk_i32 s33, 0x190
	v_lshlrev_b32_e32 v112, 4, v0
	v_lshlrev_b32_e32 v113, 4, v1
	v_lshlrev_b32_e32 v114, 4, v2
	v_lshlrev_b32_e32 v115, 4, v3
	v_lshlrev_b32_e32 v116, 4, v8
	v_lshlrev_b32_e32 v117, 4, v9
	v_lshlrev_b32_e32 v118, 4, v10
	v_lshlrev_b32_e32 v119, 4, v11
	v_lshlrev_b32_e32 v135, 2, v0
	v_add_u32_e32 v136, 0, v135
	v_mul_u32_u24_e32 v137, s34, v136
	v_lshrrev_b32_e32 v137, 16, v137
	v_mul_u32_u24_e32 v138, 3, v137
	v_sub_u32_e32 v138, v136, v138
	v_mad_u32_u24 v138, v138, s35, v137
	v_lshlrev_b32_e32 v4, 2, v138
	v_add_u32_e32 v136, 1, v135
	v_mul_u32_u24_e32 v137, s34, v136
	v_lshrrev_b32_e32 v137, 16, v137
	v_mul_u32_u24_e32 v138, 3, v137
	v_sub_u32_e32 v138, v136, v138
	v_mad_u32_u24 v138, v138, s35, v137
	v_lshlrev_b32_e32 v5, 2, v138
	v_add_u32_e32 v136, 2, v135
	v_mul_u32_u24_e32 v137, s34, v136
	v_lshrrev_b32_e32 v137, 16, v137
	v_mul_u32_u24_e32 v138, 3, v137
	v_sub_u32_e32 v138, v136, v138
	v_mad_u32_u24 v138, v138, s35, v137
	v_lshlrev_b32_e32 v6, 2, v138
	v_add_u32_e32 v136, 3, v135
	v_mul_u32_u24_e32 v137, s34, v136
	v_lshrrev_b32_e32 v137, 16, v137
	v_mul_u32_u24_e32 v138, 3, v137
	v_sub_u32_e32 v138, v136, v138
	v_mad_u32_u24 v138, v138, s35, v137
	v_lshlrev_b32_e32 v7, 2, v138
	s_waitcnt vmcnt(0)
	v_cmp_gt_u32_e32 vcc, 0x4b, v0
	s_and_saveexec_b64 s[14:15], vcc
	ds_write_b32 v4, v124 offset:12800
	ds_write_b32 v5, v125 offset:12800
	ds_write_b32 v6, v126 offset:12800
	ds_write_b32 v7, v127 offset:12800
	s_or_b64 exec, exec, s[14:15]
	v_lshlrev_b32_e32 v12, 2, v12
	v_lshlrev_b32_e32 v13, 2, v13
	v_lshlrev_b32_e32 v14, 2, v14
	v_lshlrev_b32_e32 v15, 2, v15
	global_load_dword v12, v12, s[8:9]
	global_load_dword v13, v13, s[8:9]
	global_load_dword v14, v14, s[8:9]
	global_load_dword v15, v15, s[8:9]
	s_waitcnt vmcnt(0)
	v_add_u32_e32 v12, s32, v12
	v_add_u32_e32 v13, s32, v13
	v_add_u32_e32 v14, s32, v14
	v_add_u32_e32 v15, s32, v15
	v_mad_u32_u24 v120, v12, s33, v116
	v_mad_u32_u24 v121, v13, s33, v117
	v_mad_u32_u24 v122, v14, s33, v118
	v_mad_u32_u24 v123, v15, s33, v119
	global_load_dwordx4 v[16:19], v120, s[10:11]
	global_load_dwordx4 v[20:23], v116, s[16:17]
	global_load_dwordx4 v[24:27], v112, s[24:25]
	global_load_dwordx4 v[28:31], v112, s[26:27]
	global_load_dwordx4 v[32:35], v112, s[28:29]
	global_load_dwordx4 v[36:39], v112, s[30:31]
	global_load_dwordx4 v[40:43], v121, s[10:11]
	global_load_dwordx4 v[44:47], v117, s[16:17]
	global_load_dwordx4 v[48:51], v113, s[24:25]
	global_load_dwordx4 v[52:55], v113, s[26:27]
	global_load_dwordx4 v[56:59], v113, s[28:29]
	global_load_dwordx4 v[60:63], v113, s[30:31]
	global_load_dwordx4 v[64:67], v122, s[10:11]
	global_load_dwordx4 v[68:71], v118, s[16:17]
	global_load_dwordx4 v[72:75], v114, s[24:25]
	global_load_dwordx4 v[76:79], v114, s[26:27]
	global_load_dwordx4 v[80:83], v114, s[28:29]
	global_load_dwordx4 v[84:87], v114, s[30:31]
	global_load_dwordx4 v[88:91], v123, s[10:11]
	global_load_dwordx4 v[92:95], v119, s[16:17]
	global_load_dwordx4 v[96:99], v115, s[24:25]
	global_load_dwordx4 v[100:103], v115, s[26:27]
	global_load_dwordx4 v[104:107], v115, s[28:29]
	global_load_dwordx4 v[108:111], v115, s[30:31]
	s_waitcnt vmcnt(18)
	v_pk_add_f32 v[24:25], v[24:25], v[28:29]
	v_pk_add_f32 v[26:27], v[26:27], v[30:31]
	v_pk_add_f32 v[32:33], v[32:33], v[36:37]
	v_pk_add_f32 v[34:35], v[34:35], v[38:39]
	v_pk_add_f32 v[24:25], v[24:25], v[32:33]
	v_pk_add_f32 v[26:27], v[26:27], v[34:35]
	v_pk_add_f32 v[16:17], v[20:21], v[16:17]
	v_pk_add_f32 v[18:19], v[22:23], v[18:19]
	v_pk_add_f32 v[24:25], v[24:25], v[16:17]
	v_pk_add_f32 v[26:27], v[26:27], v[18:19]
	v_max_f32_e32 v24, 0, v24
	v_max_f32_e32 v25, 0, v25
	v_max_f32_e32 v26, 0, v26
	v_max_f32_e32 v27, 0, v27
	ds_write_b128 v112, v[24:27]
	s_waitcnt vmcnt(12)
	v_pk_add_f32 v[48:49], v[48:49], v[52:53]
	v_pk_add_f32 v[50:51], v[50:51], v[54:55]
	v_pk_add_f32 v[56:57], v[56:57], v[60:61]
	v_pk_add_f32 v[58:59], v[58:59], v[62:63]
	v_pk_add_f32 v[48:49], v[48:49], v[56:57]
	v_pk_add_f32 v[50:51], v[50:51], v[58:59]
	v_pk_add_f32 v[40:41], v[44:45], v[40:41]
	v_pk_add_f32 v[42:43], v[46:47], v[42:43]
	v_pk_add_f32 v[48:49], v[48:49], v[40:41]
	v_pk_add_f32 v[50:51], v[50:51], v[42:43]
	v_max_f32_e32 v48, 0, v48
	v_max_f32_e32 v49, 0, v49
	v_max_f32_e32 v50, 0, v50
	v_max_f32_e32 v51, 0, v51
	ds_write_b128 v113, v[48:51]
	s_waitcnt vmcnt(6)
	v_pk_add_f32 v[72:73], v[72:73], v[76:77]
	v_pk_add_f32 v[74:75], v[74:75], v[78:79]
	v_pk_add_f32 v[80:81], v[80:81], v[84:85]
	v_pk_add_f32 v[82:83], v[82:83], v[86:87]
	v_pk_add_f32 v[72:73], v[72:73], v[80:81]
	v_pk_add_f32 v[74:75], v[74:75], v[82:83]
	v_pk_add_f32 v[64:65], v[68:69], v[64:65]
	v_pk_add_f32 v[66:67], v[70:71], v[66:67]
	v_pk_add_f32 v[72:73], v[72:73], v[64:65]
	v_pk_add_f32 v[74:75], v[74:75], v[66:67]
	v_max_f32_e32 v72, 0, v72
	v_max_f32_e32 v73, 0, v73
	v_max_f32_e32 v74, 0, v74
	v_max_f32_e32 v75, 0, v75
	ds_write_b128 v114, v[72:75]
	s_waitcnt vmcnt(0)
	v_pk_add_f32 v[96:97], v[96:97], v[100:101]
	v_pk_add_f32 v[98:99], v[98:99], v[102:103]
	v_pk_add_f32 v[104:105], v[104:105], v[108:109]
	v_pk_add_f32 v[106:107], v[106:107], v[110:111]
	v_pk_add_f32 v[96:97], v[96:97], v[104:105]
	v_pk_add_f32 v[98:99], v[98:99], v[106:107]
	v_pk_add_f32 v[88:89], v[92:93], v[88:89]
	v_pk_add_f32 v[90:91], v[94:95], v[90:91]
	v_pk_add_f32 v[96:97], v[96:97], v[88:89]
	v_pk_add_f32 v[98:99], v[98:99], v[90:91]
	v_max_f32_e32 v96, 0, v96
	v_max_f32_e32 v97, 0, v97
	v_max_f32_e32 v98, 0, v98
	v_max_f32_e32 v99, 0, v99
	ds_write_b128 v115, v[96:99]
	s_mul_i32 s14, s6, 3
	v_cmp_gt_i32_e32 vcc, s14, v0
	s_waitcnt lgkmcnt(0)
	s_barrier
	s_and_saveexec_b64 s[2:3], vcc
	s_cbranch_execz .LBB4_17
	v_mul_u32_u24_e32 v4, s33, v130
	v_mul_u32_u24_e32 v5, s33, v131
	ds_read_b128 v[16:19], v4 offset:0
	ds_read_b128 v[36:39], v5 offset:12800
	ds_read_b128 v[20:23], v4 offset:16
	ds_read_b128 v[40:43], v5 offset:12816
	ds_read_b128 v[24:27], v4 offset:32
	ds_read_b128 v[44:47], v5 offset:12832
	ds_read_b128 v[28:31], v4 offset:48
	ds_read_b128 v[48:51], v5 offset:12848
	ds_read_b128 v[32:35], v4 offset:64
	ds_read_b128 v[52:55], v5 offset:12864
	ds_read_b128 v[56:59], v4 offset:80
	ds_read_b128 v[76:79], v5 offset:12880
	ds_read_b128 v[60:63], v4 offset:96
	ds_read_b128 v[80:83], v5 offset:12896
	ds_read_b128 v[64:67], v4 offset:112
	ds_read_b128 v[84:87], v5 offset:12912
	ds_read_b128 v[68:71], v4 offset:128
	ds_read_b128 v[88:91], v5 offset:12928
	ds_read_b128 v[72:75], v4 offset:144
	ds_read_b128 v[92:95], v5 offset:12944
	s_waitcnt lgkmcnt(10)
	v_fmac_f32_e32 v128, v16, v36
	v_fmac_f32_e32 v128, v17, v37
	v_fmac_f32_e32 v128, v18, v38
	v_fmac_f32_e32 v128, v19, v39
	v_fmac_f32_e32 v128, v20, v40
	v_fmac_f32_e32 v128, v21, v41
	v_fmac_f32_e32 v128, v22, v42
	v_fmac_f32_e32 v128, v23, v43
	v_fmac_f32_e32 v128, v24, v44
	v_fmac_f32_e32 v128, v25, v45
	v_fmac_f32_e32 v128, v26, v46
	v_fmac_f32_e32 v128, v27, v47
	v_fmac_f32_e32 v128, v28, v48
	v_fmac_f32_e32 v128, v29, v49
	v_fmac_f32_e32 v128, v30, v50
	v_fmac_f32_e32 v128, v31, v51
	v_fmac_f32_e32 v128, v32, v52
	v_fmac_f32_e32 v128, v33, v53
	v_fmac_f32_e32 v128, v34, v54
	v_fmac_f32_e32 v128, v35, v55
	ds_read_b128 v[16:19], v4 offset:160
	ds_read_b128 v[36:39], v5 offset:12960
	ds_read_b128 v[20:23], v4 offset:176
	ds_read_b128 v[40:43], v5 offset:12976
	ds_read_b128 v[24:27], v4 offset:192
	ds_read_b128 v[44:47], v5 offset:12992
	ds_read_b128 v[28:31], v4 offset:208
	ds_read_b128 v[48:51], v5 offset:13008
	ds_read_b128 v[32:35], v4 offset:224
	ds_read_b128 v[52:55], v5 offset:13024
	s_waitcnt lgkmcnt(10)
	v_fmac_f32_e32 v128, v56, v76
	v_fmac_f32_e32 v128, v57, v77
	v_fmac_f32_e32 v128, v58, v78
	v_fmac_f32_e32 v128, v59, v79
	v_fmac_f32_e32 v128, v60, v80
	v_fmac_f32_e32 v128, v61, v81
	v_fmac_f32_e32 v128, v62, v82
	v_fmac_f32_e32 v128, v63, v83
	v_fmac_f32_e32 v128, v64, v84
	v_fmac_f32_e32 v128, v65, v85
	v_fmac_f32_e32 v128, v66, v86
	v_fmac_f32_e32 v128, v67, v87
	v_fmac_f32_e32 v128, v68, v88
	v_fmac_f32_e32 v128, v69, v89
	v_fmac_f32_e32 v128, v70, v90
	v_fmac_f32_e32 v128, v71, v91
	v_fmac_f32_e32 v128, v72, v92
	v_fmac_f32_e32 v128, v73, v93
	v_fmac_f32_e32 v128, v74, v94
	v_fmac_f32_e32 v128, v75, v95
	ds_read_b128 v[56:59], v4 offset:240
	ds_read_b128 v[76:79], v5 offset:13040
	ds_read_b128 v[60:63], v4 offset:256
	ds_read_b128 v[80:83], v5 offset:13056
	ds_read_b128 v[64:67], v4 offset:272
	ds_read_b128 v[84:87], v5 offset:13072
	ds_read_b128 v[68:71], v4 offset:288
	ds_read_b128 v[88:91], v5 offset:13088
	ds_read_b128 v[72:75], v4 offset:304
	ds_read_b128 v[92:95], v5 offset:13104
	s_waitcnt lgkmcnt(10)
	v_fmac_f32_e32 v128, v16, v36
	v_fmac_f32_e32 v128, v17, v37
	v_fmac_f32_e32 v128, v18, v38
	v_fmac_f32_e32 v128, v19, v39
	v_fmac_f32_e32 v128, v20, v40
	v_fmac_f32_e32 v128, v21, v41
	v_fmac_f32_e32 v128, v22, v42
	v_fmac_f32_e32 v128, v23, v43
	v_fmac_f32_e32 v128, v24, v44
	v_fmac_f32_e32 v128, v25, v45
	v_fmac_f32_e32 v128, v26, v46
	v_fmac_f32_e32 v128, v27, v47
	v_fmac_f32_e32 v128, v28, v48
	v_fmac_f32_e32 v128, v29, v49
	v_fmac_f32_e32 v128, v30, v50
	v_fmac_f32_e32 v128, v31, v51
	v_fmac_f32_e32 v128, v32, v52
	v_fmac_f32_e32 v128, v33, v53
	v_fmac_f32_e32 v128, v34, v54
	v_fmac_f32_e32 v128, v35, v55
	ds_read_b128 v[16:19], v4 offset:320
	ds_read_b128 v[36:39], v5 offset:13120
	ds_read_b128 v[20:23], v4 offset:336
	ds_read_b128 v[40:43], v5 offset:13136
	ds_read_b128 v[24:27], v4 offset:352
	ds_read_b128 v[44:47], v5 offset:13152
	ds_read_b128 v[28:31], v4 offset:368
	ds_read_b128 v[48:51], v5 offset:13168
	ds_read_b128 v[32:35], v4 offset:384
	ds_read_b128 v[52:55], v5 offset:13184
	s_waitcnt lgkmcnt(10)
	v_fmac_f32_e32 v128, v56, v76
	v_fmac_f32_e32 v128, v57, v77
	v_fmac_f32_e32 v128, v58, v78
	v_fmac_f32_e32 v128, v59, v79
	v_fmac_f32_e32 v128, v60, v80
	v_fmac_f32_e32 v128, v61, v81
	v_fmac_f32_e32 v128, v62, v82
	v_fmac_f32_e32 v128, v63, v83
	v_fmac_f32_e32 v128, v64, v84
	v_fmac_f32_e32 v128, v65, v85
	v_fmac_f32_e32 v128, v66, v86
	v_fmac_f32_e32 v128, v67, v87
	v_fmac_f32_e32 v128, v68, v88
	v_fmac_f32_e32 v128, v69, v89
	v_fmac_f32_e32 v128, v70, v90
	v_fmac_f32_e32 v128, v71, v91
	v_fmac_f32_e32 v128, v72, v92
	v_fmac_f32_e32 v128, v73, v93
	v_fmac_f32_e32 v128, v74, v94
	v_fmac_f32_e32 v128, v75, v95
	s_waitcnt lgkmcnt(0)
	v_fmac_f32_e32 v128, v16, v36
	v_fmac_f32_e32 v128, v17, v37
	v_fmac_f32_e32 v128, v18, v38
	v_fmac_f32_e32 v128, v19, v39
	v_fmac_f32_e32 v128, v20, v40
	v_fmac_f32_e32 v128, v21, v41
	v_fmac_f32_e32 v128, v22, v42
	v_fmac_f32_e32 v128, v23, v43
	v_fmac_f32_e32 v128, v24, v44
	v_fmac_f32_e32 v128, v25, v45
	v_fmac_f32_e32 v128, v26, v46
	v_fmac_f32_e32 v128, v27, v47
	v_fmac_f32_e32 v128, v28, v48
	v_fmac_f32_e32 v128, v29, v49
	v_fmac_f32_e32 v128, v30, v50
	v_fmac_f32_e32 v128, v31, v51
	v_fmac_f32_e32 v128, v32, v52
	v_fmac_f32_e32 v128, v33, v53
	v_fmac_f32_e32 v128, v34, v54
	v_fmac_f32_e32 v128, v35, v55
	v_mul_u32_u24_e32 v6, 3, v129
	v_add_lshl_u32 v6, v6, v131, 2
	global_store_dword v6, v128, s[40:41]

	.amdhsa_kernel _Z12final_kernelPKfPKiPK15HIP_vector_typeIiLj4EES2_S2_S0_S0_S0_S0_Pf
		.amdhsa_group_segment_fixed_size 14000
		.amdhsa_private_segment_fixed_size 0
		.amdhsa_kernarg_size 80
		.amdhsa_user_sgpr_count 2
		.amdhsa_user_sgpr_dispatch_ptr 0
		.amdhsa_user_sgpr_queue_ptr 0
		.amdhsa_user_sgpr_kernarg_segment_ptr 1
		.amdhsa_user_sgpr_dispatch_id 0
		.amdhsa_user_sgpr_kernarg_preload_length 0
		.amdhsa_user_sgpr_kernarg_preload_offset 0
		.amdhsa_user_sgpr_private_segment_size 0
		.amdhsa_uses_dynamic_stack 0
		.amdhsa_enable_private_segment 0
		.amdhsa_system_sgpr_workgroup_id_x 1
		.amdhsa_system_sgpr_workgroup_id_y 0
		.amdhsa_system_sgpr_workgroup_id_z 0
		.amdhsa_system_sgpr_workgroup_info 0
		.amdhsa_system_vgpr_workitem_id 0
		.amdhsa_next_free_vgpr 140
		.amdhsa_next_free_sgpr 44
		.amdhsa_accum_offset 140
		.amdhsa_reserve_vcc 1
		.amdhsa_float_round_mode_32 0
		.amdhsa_float_round_mode_16_64 0
		.amdhsa_float_denorm_mode_32 3
		.amdhsa_float_denorm_mode_16_64 3
		.amdhsa_dx10_clamp 1
		.amdhsa_ieee_mode 1
		.amdhsa_fp16_overflow 0
		.amdhsa_tg_split 0
		.amdhsa_exception_fp_ieee_invalid_op 0
		.amdhsa_exception_fp_denorm_src 0
		.amdhsa_exception_fp_ieee_div_zero 0
		.amdhsa_exception_fp_ieee_overflow 0
		.amdhsa_exception_fp_ieee_underflow 0
		.amdhsa_exception_fp_ieee_inexact 0
		.amdhsa_exception_int_div_zero 0
	.end_amdhsa_kernel

amdhsa.kernels:
  - .agpr_count:     0
    .args:
      - .actual_access:  read_only
        .address_space:  global
        .offset:         0
        .size:           8
        .value_kind:     global_buffer
      - .actual_access:  write_only
        .address_space:  global
        .offset:         8
        .size:           8
        .value_kind:     global_buffer
      - .actual_access:  read_only
        .address_space:  global
        .offset:         16
        .size:           8
        .value_kind:     global_buffer
      - .actual_access:  read_only
        .address_space:  global
        .offset:         24
        .size:           8
        .value_kind:     global_buffer
      - .actual_access:  read_only
        .address_space:  global
        .offset:         32
        .size:           8
        .value_kind:     global_buffer
      - .actual_access:  write_only
        .address_space:  global
        .offset:         40
        .size:           8
        .value_kind:     global_buffer
      - .actual_access:  write_only
        .address_space:  global
        .offset:         48
        .size:           8
        .value_kind:     global_buffer
      - .actual_access:  write_only
        .address_space:  global
        .offset:         56
        .size:           8
        .value_kind:     global_buffer
      - .actual_access:  write_only
        .address_space:  global
        .offset:         64
        .size:           8
        .value_kind:     global_buffer
      - .actual_access:  write_only
        .address_space:  global
        .offset:         72
        .size:           8
        .value_kind:     global_buffer
      - .actual_access:  write_only
        .address_space:  global
        .offset:         80
        .size:           8
        .value_kind:     global_buffer
    .group_segment_fixed_size: 16640
    .kernarg_segment_align: 8
    .kernarg_segment_size: 88
    .language:       OpenCL C
    .language_version:
      - 2
      - 0
    .max_flat_workgroup_size: 256
    .name:           _Z8prep_allPKfPcS0_S0_S0_S1_S1_S1_PyPiS3_
    .private_segment_fixed_size: 0
    .sgpr_count:     30
    .sgpr_spill_count: 0
    .symbol:         _Z8prep_allPKfPcS0_S0_S0_S1_S1_S1_PyPiS3_.kd
    .uniform_work_group_size: 1
    .uses_dynamic_stack: false
    .vgpr_count:     48
    .vgpr_spill_count: 0
    .wavefront_size: 64
  - .agpr_count:     0
    .args:
      - .actual_access:  read_only
        .address_space:  global
        .offset:         0
        .size:           8
        .value_kind:     global_buffer
      - .actual_access:  write_only
        .address_space:  global
        .offset:         8
        .size:           8
        .value_kind:     global_buffer
      - .actual_access:  write_only
        .address_space:  global
        .offset:         16
        .size:           8
        .value_kind:     global_buffer
      - .address_space:  global
        .offset:         24
        .size:           8
        .value_kind:     global_buffer
    .group_segment_fixed_size: 0
    .kernarg_segment_align: 8
    .kernarg_segment_size: 32
    .language:       OpenCL C
    .language_version:
      - 2
      - 0
    .max_flat_workgroup_size: 256
    .name:           _Z13select_kernelPKfPyPiS2_
    .private_segment_fixed_size: 0
    .sgpr_count:     21
    .sgpr_spill_count: 0
    .symbol:         _Z13select_kernelPKfPyPiS2_.kd
    .uniform_work_group_size: 1
    .uses_dynamic_stack: false
    .vgpr_count:     12
    .vgpr_spill_count: 0
    .wavefront_size: 64
  - .agpr_count:     0
    .args:
      - .actual_access:  read_only
        .address_space:  global
        .offset:         0
        .size:           8
        .value_kind:     global_buffer
      - .actual_access:  write_only
        .address_space:  global
        .offset:         8
        .size:           8
        .value_kind:     global_buffer
      - .actual_access:  write_only
        .address_space:  global
        .offset:         16
        .size:           8
        .value_kind:     global_buffer
      - .actual_access:  write_only
        .address_space:  global
        .offset:         24
        .size:           8
        .value_kind:     global_buffer
    .group_segment_fixed_size: 4128
    .kernarg_segment_align: 8
    .kernarg_segment_size: 32
    .language:       OpenCL C
    .language_version:
      - 2
      - 0
    .max_flat_workgroup_size: 1024
    .name:           _Z12route_kernelPKyPiP15HIP_vector_typeIiLj4EES1_
    .private_segment_fixed_size: 0
    .sgpr_count:     19
    .sgpr_spill_count: 0
    .symbol:         _Z12route_kernelPKyPiP15HIP_vector_typeIiLj4EES1_.kd
    .uniform_work_group_size: 1
    .uses_dynamic_stack: false
    .vgpr_count:     23
    .vgpr_spill_count: 0
    .wavefront_size: 64
  - .agpr_count:     66
    .args:
      - .actual_access:  read_only
        .address_space:  global
        .offset:         0
        .size:           8
        .value_kind:     global_buffer
      - .actual_access:  read_only
        .address_space:  global
        .offset:         8
        .size:           8
        .value_kind:     global_buffer
      - .actual_access:  read_only
        .address_space:  global
        .offset:         16
        .size:           8
        .value_kind:     global_buffer
      - .actual_access:  read_only
        .address_space:  global
        .offset:         24
        .size:           8
        .value_kind:     global_buffer
      - .actual_access:  read_only
        .address_space:  global
        .offset:         32
        .size:           8
        .value_kind:     global_buffer
      - .actual_access:  write_only
        .address_space:  global
        .offset:         40
        .size:           8
        .value_kind:     global_buffer
    .group_segment_fixed_size: 51200
    .kernarg_segment_align: 8
    .kernarg_segment_size: 48
    .language:       OpenCL C
    .language_version:
      - 2
      - 0
    .max_flat_workgroup_size: 256
    .name:           _Z13expert_kernelPKcPKfPKiPK15HIP_vector_typeIiLj4EES4_Pf
    .private_segment_fixed_size: 0
    .sgpr_count:     20
    .sgpr_spill_count: 0
    .symbol:         _Z13expert_kernelPKcPKfPKiPK15HIP_vector_typeIiLj4EES4_Pf.kd
    .uniform_work_group_size: 1
    .uses_dynamic_stack: false
    .vgpr_count:     154
    .vgpr_spill_count: 0
    .wavefront_size: 64
  - .agpr_count:     0
    .args:
      - .actual_access:  read_only
        .address_space:  global
        .offset:         0
        .size:           8
        .value_kind:     global_buffer
      - .actual_access:  read_only
        .address_space:  global
        .offset:         8
        .size:           8
        .value_kind:     global_buffer
      - .actual_access:  read_only
        .address_space:  global
        .offset:         16
        .size:           8
        .value_kind:     global_buffer
      - .actual_access:  read_only
        .address_space:  global
        .offset:         24
        .size:           8
        .value_kind:     global_buffer
      - .actual_access:  read_only
        .address_space:  global
        .offset:         32
        .size:           8
        .value_kind:     global_buffer
      - .actual_access:  read_only
        .address_space:  global
        .offset:         40
        .size:           8
        .value_kind:     global_buffer
      - .actual_access:  read_only
        .address_space:  global
        .offset:         48
        .size:           8
        .value_kind:     global_buffer
      - .actual_access:  read_only
        .address_space:  global
        .offset:         56
        .size:           8
        .value_kind:     global_buffer
      - .actual_access:  read_only
        .address_space:  global
        .offset:         64
        .size:           8
        .value_kind:     global_buffer
      - .actual_access:  write_only
        .address_space:  global
        .offset:         72
        .size:           8
        .value_kind:     global_buffer
    .group_segment_fixed_size: 14000
    .kernarg_segment_align: 8
    .kernarg_segment_size: 80
    .language:       OpenCL C
    .language_version:
      - 2
      - 0
    .max_flat_workgroup_size: 256
    .name:           _Z12final_kernelPKfPKiPK15HIP_vector_typeIiLj4EES2_S2_S0_S0_S0_S0_Pf
    .private_segment_fixed_size: 0
    .sgpr_count:     50
    .sgpr_spill_count: 0
    .symbol:         _Z12final_kernelPKfPKiPK15HIP_vector_typeIiLj4EES2_S2_S0_S0_S0_S0_Pf.kd
    .uniform_work_group_size: 1
    .uses_dynamic_stack: false
    .vgpr_count:     140
    .vgpr_spill_count: 0
    .wavefront_size: 64
  - .agpr_count:     0
    .args:
      - .address_space:  global
        .offset:         0
        .size:           8
        .value_kind:     global_buffer
      - .address_space:  global
        .offset:         8
        .size:           8
        .value_kind:     global_buffer
      - .offset:         16
        .size:           4
        .value_kind:     by_value
      - .offset:         20
        .size:           4
        .value_kind:     by_value
      - .actual_access:  read_only
        .address_space:  global
        .offset:         24
        .size:           8
        .value_kind:     global_buffer
      - .offset:         32
        .size:           4
        .value_kind:     by_value
      - .actual_access:  read_only
        .address_space:  global
        .offset:         40
        .size:           8
        .value_kind:     global_buffer
      - .actual_access:  read_only
        .address_space:  global
        .offset:         48
        .size:           8
        .value_kind:     global_buffer
      - .actual_access:  write_only
        .address_space:  global
        .offset:         56
        .size:           8
        .value_kind:     global_buffer
      - .offset:         64
        .size:           4
        .value_kind:     by_value
      - .actual_access:  read_only
        .address_space:  global
        .offset:         72
        .size:           8
        .value_kind:     global_buffer
    .group_segment_fixed_size: 0
    .kernarg_segment_align: 8
    .kernarg_segment_size: 80
    .language:       OpenCL C
    .language_version:
      - 2
      - 0
    .max_flat_workgroup_size: 512
    .name:           _Z7gemm_x3ILi2ELi2ELi2ELi0EEvPKcS1_iiPKfiS3_PKiPciPy
    .private_segment_fixed_size: 0
    .sgpr_count:     38
    .sgpr_spill_count: 0
    .symbol:         _Z7gemm_x3ILi2ELi2ELi2ELi0EEvPKcS1_iiPKfiS3_PKiPciPy.kd
    .uniform_work_group_size: 1
    .uses_dynamic_stack: false
    .vgpr_count:     208
    .vgpr_spill_count: 0
    .wavefront_size: 64
  - .agpr_count:     0
    .args:
      - .address_space:  global
        .offset:         0
        .size:           8
        .value_kind:     global_buffer
      - .address_space:  global
        .offset:         8
        .size:           8
        .value_kind:     global_buffer
      - .offset:         16
        .size:           4
        .value_kind:     by_value
      - .offset:         20
        .size:           4
        .value_kind:     by_value
      - .actual_access:  read_only
        .address_space:  global
        .offset:         24
        .size:           8
        .value_kind:     global_buffer
      - .offset:         32
        .size:           4
        .value_kind:     by_value
      - .actual_access:  read_only
        .address_space:  global
        .offset:         40
        .size:           8
        .value_kind:     global_buffer
      - .actual_access:  read_only
        .address_space:  global
        .offset:         48
        .size:           8
        .value_kind:     global_buffer
      - .actual_access:  write_only
        .address_space:  global
        .offset:         56
        .size:           8
        .value_kind:     global_buffer
      - .offset:         64
        .size:           4
        .value_kind:     by_value
      - .actual_access:  read_only
        .address_space:  global
        .offset:         72
        .size:           8
        .value_kind:     global_buffer
    .group_segment_fixed_size: 0
    .kernarg_segment_align: 8
    .kernarg_segment_size: 80
    .language:       OpenCL C
    .language_version:
      - 2
      - 0
    .max_flat_workgroup_size: 512
    .name:           _Z7gemm_x3ILi2ELi2ELi1ELi1EEvPKcS1_iiPKfiS3_PKiPciPy
    .private_segment_fixed_size: 0
    .sgpr_count:     32
    .sgpr_spill_count: 0
    .symbol:         _Z7gemm_x3ILi2ELi2ELi1ELi1EEvPKcS1_iiPKfiS3_PKiPciPy.kd
    .uniform_work_group_size: 1
    .uses_dynamic_stack: false
    .vgpr_count:     114
    .vgpr_spill_count: 0
    .wavefront_size: 64
  - .agpr_count:     32
    .args:
      - .address_space:  global
        .offset:         0
        .size:           8
        .value_kind:     global_buffer
      - .address_space:  global
        .offset:         8
        .size:           8
        .value_kind:     global_buffer
      - .offset:         16
        .size:           4
        .value_kind:     by_value
      - .offset:         20
        .size:           4
        .value_kind:     by_value
      - .actual_access:  read_only
        .address_space:  global
        .offset:         24
        .size:           8
        .value_kind:     global_buffer
      - .offset:         32
        .size:           4
        .value_kind:     by_value
      - .actual_access:  read_only
        .address_space:  global
        .offset:         40
        .size:           8
        .value_kind:     global_buffer
      - .actual_access:  read_only
        .address_space:  global
        .offset:         48
        .size:           8
        .value_kind:     global_buffer
      - .actual_access:  write_only
        .address_space:  global
        .offset:         56
        .size:           8
        .value_kind:     global_buffer
      - .offset:         64
        .size:           4
        .value_kind:     by_value
      - .address_space:  global
        .offset:         72
        .size:           8
        .value_kind:     global_buffer
    .group_segment_fixed_size: 0
    .kernarg_segment_align: 8
    .kernarg_segment_size: 80
    .language:       OpenCL C
    .language_version:
      - 2
      - 0
    .max_flat_workgroup_size: 256
    .name:           _Z7gemm_x3ILi1ELi2ELi1ELi2EEvPKcS1_iiPKfiS3_PKiPciPy
    .private_segment_fixed_size: 0
    .sgpr_count:     29
    .sgpr_spill_count: 0
    .symbol:         _Z7gemm_x3ILi1ELi2ELi1ELi2EEvPKcS1_iiPKfiS3_PKiPciPy.kd
    .uniform_work_group_size: 1
    .uses_dynamic_stack: false
    .vgpr_count:     136
    .vgpr_spill_count: 0
    .wavefront_size: 64
  - .agpr_count:     0
    .args:
      - .actual_access:  read_only
        .address_space:  global
        .offset:         0
        .size:           8
        .value_kind:     global_buffer
      - .offset:         8
        .size:           4
        .value_kind:     by_value
      - .offset:         12
        .size:           4
        .value_kind:     by_value
      - .actual_access:  read_only
        .address_space:  global
        .offset:         16
        .size:           8
        .value_kind:     global_buffer
      - .offset:         24
        .size:           4
        .value_kind:     by_value
      - .offset:         28
        .size:           4
        .value_kind:     by_value
      - .actual_access:  read_only
        .address_space:  global
        .offset:         32
        .size:           8
        .value_kind:     global_buffer
      - .actual_access:  read_only
        .address_space:  global
        .offset:         40
        .size:           8
        .value_kind:     global_buffer
      - .actual_access:  read_only
        .address_space:  global
        .offset:         48
        .size:           8
        .value_kind:     global_buffer
      - .actual_access:  read_only
        .address_space:  global
        .offset:         56
        .size:           8
        .value_kind:     global_buffer
      - .actual_access:  write_only
        .address_space:  global
        .offset:         64
        .size:           8
        .value_kind:     global_buffer
      - .offset:         72
        .size:           4
        .value_kind:     by_value
      - .actual_access:  read_only
        .address_space:  global
        .offset:         80
        .size:           8
        .value_kind:     global_buffer
      - .offset:         88
        .size:           4
        .value_kind:     hidden_block_count_x
      - .offset:         92
        .size:           4
        .value_kind:     hidden_block_count_y
      - .offset:         96
        .size:           4
        .value_kind:     hidden_block_count_z
      - .offset:         100
        .size:           2
        .value_kind:     hidden_group_size_x
      - .offset:         102
        .size:           2
        .value_kind:     hidden_group_size_y
      - .offset:         104
        .size:           2
        .value_kind:     hidden_group_size_z
      - .offset:         106
        .size:           2
        .value_kind:     hidden_remainder_x
      - .offset:         108
        .size:           2
        .value_kind:     hidden_remainder_y
      - .offset:         110
        .size:           2
        .value_kind:     hidden_remainder_z
      - .offset:         128
        .size:           8
        .value_kind:     hidden_global_offset_x
      - .offset:         136
        .size:           8
        .value_kind:     hidden_global_offset_y
      - .offset:         144
        .size:           8
        .value_kind:     hidden_global_offset_z
      - .offset:         152
        .size:           2
        .value_kind:     hidden_grid_dims
    .group_segment_fixed_size: 16384
    .kernarg_segment_align: 8
    .kernarg_segment_size: 344
    .language:       OpenCL C
    .language_version:
      - 2
      - 0
    .max_flat_workgroup_size: 1024
    .name:           _Z13refine_kernelILi1ELi16ELi128ELb1ELi4EEvPKfiiS1_iiS1_PKiS3_S3_PfiPy
    .private_segment_fixed_size: 0
    .sgpr_count:     35
    .sgpr_spill_count: 0
    .symbol:         _Z13refine_kernelILi1ELi16ELi128ELb1ELi4EEvPKfiiS1_iiS1_PKiS3_S3_PfiPy.kd
    .uniform_work_group_size: 1
    .uses_dynamic_stack: false
    .vgpr_count:     64
    .vgpr_spill_count: 0
    .wavefront_size: 64
  - .agpr_count:     0
    .args:
      - .actual_access:  read_only
        .address_space:  global
        .offset:         0
        .size:           8
        .value_kind:     global_buffer
      - .offset:         8
        .size:           4
        .value_kind:     by_value
      - .offset:         12
        .size:           4
        .value_kind:     by_value
      - .actual_access:  read_only
        .address_space:  global
        .offset:         16
        .size:           8
        .value_kind:     global_buffer
      - .offset:         24
        .size:           4
        .value_kind:     by_value
      - .offset:         28
        .size:           4
        .value_kind:     by_value
      - .actual_access:  read_only
        .address_space:  global
        .offset:         32
        .size:           8
        .value_kind:     global_buffer
      - .actual_access:  read_only
        .address_space:  global
        .offset:         40
        .size:           8
        .value_kind:     global_buffer
      - .actual_access:  read_only
        .address_space:  global
        .offset:         48
        .size:           8
        .value_kind:     global_buffer
      - .actual_access:  read_only
        .address_space:  global
        .offset:         56
        .size:           8
        .value_kind:     global_buffer
      - .actual_access:  write_only
        .address_space:  global
        .offset:         64
        .size:           8
        .value_kind:     global_buffer
      - .offset:         72
        .size:           4
        .value_kind:     by_value
      - .actual_access:  read_only
        .address_space:  global
        .offset:         80
        .size:           8
        .value_kind:     global_buffer
      - .offset:         88
        .size:           4
        .value_kind:     hidden_block_count_x
      - .offset:         92
        .size:           4
        .value_kind:     hidden_block_count_y
      - .offset:         96
        .size:           4
        .value_kind:     hidden_block_count_z
      - .offset:         100
        .size:           2
        .value_kind:     hidden_group_size_x
      - .offset:         102
        .size:           2
        .value_kind:     hidden_group_size_y
      - .offset:         104
        .size:           2
        .value_kind:     hidden_group_size_z
      - .offset:         106
        .size:           2
        .value_kind:     hidden_remainder_x
      - .offset:         108
        .size:           2
        .value_kind:     hidden_remainder_y
      - .offset:         110
        .size:           2
        .value_kind:     hidden_remainder_z
      - .offset:         128
        .size:           8
        .value_kind:     hidden_global_offset_x
      - .offset:         136
        .size:           8
        .value_kind:     hidden_global_offset_y
      - .offset:         144
        .size:           8
        .value_kind:     hidden_global_offset_z
      - .offset:         152
        .size:           2
        .value_kind:     hidden_grid_dims
    .group_segment_fixed_size: 16384
    .kernarg_segment_align: 8
    .kernarg_segment_size: 344
    .language:       OpenCL C
    .language_version:
      - 2
      - 0
    .max_flat_workgroup_size: 1024
    .name:           _Z13refine_kernelILi2ELi16ELi64ELb0ELi4EEvPKfiiS1_iiS1_PKiS3_S3_PfiPy
    .private_segment_fixed_size: 0
    .sgpr_count:     35
    .sgpr_spill_count: 0
    .symbol:         _Z13refine_kernelILi2ELi16ELi64ELb0ELi4EEvPKfiiS1_iiS1_PKiS3_S3_PfiPy.kd
    .uniform_work_group_size: 1
    .uses_dynamic_stack: false
    .vgpr_count:     85
    .vgpr_spill_count: 0
    .wavefront_size: 64
  - .agpr_count:     0
    .args:
      - .actual_access:  read_only
        .address_space:  global
        .offset:         0
        .size:           8
        .value_kind:     global_buffer
      - .offset:         8
        .size:           4
        .value_kind:     by_value
      - .offset:         12
        .size:           4
        .value_kind:     by_value
      - .actual_access:  read_only
        .address_space:  global
        .offset:         16
        .size:           8
        .value_kind:     global_buffer
      - .offset:         24
        .size:           4
        .value_kind:     by_value
      - .offset:         28
        .size:           4
        .value_kind:     by_value
      - .actual_access:  read_only
        .address_space:  global
        .offset:         32
        .size:           8
        .value_kind:     global_buffer
      - .actual_access:  read_only
        .address_space:  global
        .offset:         40
        .size:           8
        .value_kind:     global_buffer
      - .actual_access:  read_only
        .address_space:  global
        .offset:         48
        .size:           8
        .value_kind:     global_buffer
      - .actual_access:  read_only
        .address_space:  global
        .offset:         56
        .size:           8
        .value_kind:     global_buffer
      - .actual_access:  read_only
        .address_space:  global
        .offset:         64
        .size:           8
        .value_kind:     global_buffer
      - .offset:         72
        .size:           4
        .value_kind:     by_value
      - .address_space:  global
        .offset:         80
        .size:           8
        .value_kind:     global_buffer
      - .offset:         88
        .size:           4
        .value_kind:     hidden_block_count_x
      - .offset:         92
        .size:           4
        .value_kind:     hidden_block_count_y
      - .offset:         96
        .size:           4
        .value_kind:     hidden_block_count_z
      - .offset:         100
        .size:           2
        .value_kind:     hidden_group_size_x
      - .offset:         102
        .size:           2
        .value_kind:     hidden_group_size_y
      - .offset:         104
        .size:           2
        .value_kind:     hidden_group_size_z
      - .offset:         106
        .size:           2
        .value_kind:     hidden_remainder_x
      - .offset:         108
        .size:           2
        .value_kind:     hidden_remainder_y
      - .offset:         110
        .size:           2
        .value_kind:     hidden_remainder_z
      - .offset:         128
        .size:           8
        .value_kind:     hidden_global_offset_x
      - .offset:         136
        .size:           8
        .value_kind:     hidden_global_offset_y
      - .offset:         144
        .size:           8
        .value_kind:     hidden_global_offset_z
      - .offset:         152
        .size:           2
        .value_kind:     hidden_grid_dims
    .group_segment_fixed_size: 8192
    .kernarg_segment_align: 8
    .kernarg_segment_size: 344
    .language:       OpenCL C
    .language_version:
      - 2
      - 0
    .max_flat_workgroup_size: 512
    .name:           _Z13refine_kernelILi3ELi8ELi64ELb0ELi4EEvPKfiiS1_iiS1_PKiS3_S3_PfiPy
    .private_segment_fixed_size: 0
    .sgpr_count:     38
    .sgpr_spill_count: 0
    .symbol:         _Z13refine_kernelILi3ELi8ELi64ELb0ELi4EEvPKfiiS1_iiS1_PKiS3_S3_PfiPy.kd
    .uniform_work_group_size: 1
    .uses_dynamic_stack: false
    .vgpr_count:     88
    .vgpr_spill_count: 0
    .wavefront_size: 64
